# attention: K loop software-pipelined (static K image: fragments of the next two key blocks read during the MFMA chain), DMA lane offsets by 24-bit mads + scalar base
# speedup vs baseline: 1.0037x; 1.0037x over previous
.LBB0_427:
	v_or_b32_e32 v3, s3, v7
	v_lshlrev_b32_e32 v3, s1, v3
	v_add_u32_e32 v180, s42, v3
	s_movk_i32 s4, 0x1880
	v_mov_b64_e32 v[10:11], s[84:85]
	v_mad_i64_i32 v[10:11], s[4:5], v180, s4, v[10:11]
	s_lshl_b32 s4, s2, 1
	s_mov_b32 s5, 0
	v_lshl_add_u64 v[10:11], v[10:11], 0, s[4:5]
	v_lshlrev_b32_e32 v12, 4, v6
	v_mov_b32_e32 v13, 0
	v_lshl_add_u64 v[10:11], v[10:11], 0, v[12:13]
	global_load_dwordx4 v[146:149], v[10:11], off offset:96
	global_load_dwordx4 v[150:153], v[10:11], off offset:64
	global_load_dwordx4 v[154:157], v[10:11], off offset:32
	global_load_dwordx4 v[158:161], v[10:11], off
	s_lshl_b32 s81, 1, s1
	s_lshl_b32 s1, 0xffffff80, s1
	s_waitcnt vmcnt(0)
	s_add_i32 s82, s42, s1
	v_lshlrev_b32_e32 v2, 4, v2
	s_movk_i32 s1, 0x1000
	v_add3_u32 v182, v1, v2, s1
	s_movk_i32 s16, 0x1880
	v_and_b32_e32 v100, 63, v0
	v_lshrrev_b32_e32 v101, 3, v100
	v_and_b32_e32 v104, 7, v100
	v_xor_b32_e32 v104, v104, v101
	v_lshlrev_b32_e32 v104, 4, v104
	s_lshl_b32 s10, s88, 7
	s_add_u32 s10, s10, 0x800
	v_add_u32_e32 v104, s10, v104
	s_bfe_u32 s11, s75, 0x2000c
	s_and_b32 s12, s75, 0xffff0000
	s_add_u32 s12, s12, 0x8000
	s_add_u32 s13, s11, 1
	s_lshl_b32 s10, s13, 5
	v_add_u32_e32 v102, s10, v101
	v_mul_u32_u24_e32 v103, s81, v102
	v_add_u32_e32 v103, s82, v103
	s_lshl_b32 s10, s13, 12
	s_add_u32 s10, s10, s12
	s_lshl_b32 s13, s81, 3
	v_max_i32_e32 v106, 0, v103
	s_mov_b32 m0, s10
	v_mad_u32_u24 v108, v106, s16, v104
	global_load_lds_dwordx4 v108, s[84:85]
	v_add_u32_e32 v103, s13, v103
	v_max_i32_e32 v106, 0, v103
	s_add_u32 m0, s10, 0x400
	v_mad_u32_u24 v108, v106, s16, v104
	global_load_lds_dwordx4 v108, s[84:85]
	v_add_u32_e32 v103, s13, v103
	v_max_i32_e32 v106, 0, v103
	s_add_u32 m0, s10, 0x800
	v_mad_u32_u24 v108, v106, s16, v104
	global_load_lds_dwordx4 v108, s[84:85]
	v_add_u32_e32 v103, s13, v103
	v_max_i32_e32 v106, 0, v103
	s_add_u32 m0, s10, 0xc00
	v_mad_u32_u24 v108, v106, s16, v104
	global_load_lds_dwordx4 v108, s[84:85]
	s_add_u32 s13, s11, 4
	s_cmp_eq_u32 s11, 0
	s_cselect_b32 s13, 0, s13
	s_lshl_b32 s10, s13, 5
	v_add_u32_e32 v102, s10, v101
	v_mul_u32_u24_e32 v103, s81, v102
	v_add_u32_e32 v103, s82, v103
	s_lshl_b32 s10, s13, 12
	s_add_u32 s10, s10, s12
	s_lshl_b32 s13, s81, 3
	v_max_i32_e32 v106, 0, v103
	s_mov_b32 m0, s10
	v_mad_u32_u24 v108, v106, s16, v104
	global_load_lds_dwordx4 v108, s[84:85]
	v_add_u32_e32 v103, s13, v103
	v_max_i32_e32 v106, 0, v103
	s_add_u32 m0, s10, 0x400
	v_mad_u32_u24 v108, v106, s16, v104
	global_load_lds_dwordx4 v108, s[84:85]
	v_add_u32_e32 v103, s13, v103
	v_max_i32_e32 v106, 0, v103
	s_add_u32 m0, s10, 0x800
	v_mad_u32_u24 v108, v106, s16, v104
	global_load_lds_dwordx4 v108, s[84:85]
	v_add_u32_e32 v103, s13, v103
	v_max_i32_e32 v106, 0, v103
	s_add_u32 m0, s10, 0xc00
	v_mad_u32_u24 v108, v106, s16, v104
	global_load_lds_dwordx4 v108, s[84:85]
	v_and_b32_e32 v100, 63, v0
	v_lshrrev_b32_e32 v101, 3, v100
	v_and_b32_e32 v104, 7, v100
	v_lshlrev_b32_e32 v104, 4, v104
	s_lshl_b32 s10, s88, 7
	s_add_u32 s10, s10, 0x1000
	v_add_u32_e32 v104, s10, v104
	s_bfe_u32 s11, s75, 0x2000c
	s_and_b32 s12, s75, 0xffff0000
	s_add_u32 s13, s11, 1
	s_lshl_b32 s10, s13, 5
	v_add_u32_e32 v102, s10, v101
	v_mul_u32_u24_e32 v103, s81, v102
	v_add_u32_e32 v103, s82, v103
	s_lshl_b32 s10, s13, 12
	s_add_u32 s10, s10, s12
	s_lshl_b32 s13, s81, 3
	v_max_i32_e32 v106, 0, v103
	s_mov_b32 m0, s10
	v_mad_u32_u24 v108, v106, s16, v104
	global_load_lds_dwordx4 v108, s[84:85]
	v_add_u32_e32 v103, s13, v103
	v_max_i32_e32 v106, 0, v103
	s_add_u32 m0, s10, 0x400
	v_mad_u32_u24 v108, v106, s16, v104
	global_load_lds_dwordx4 v108, s[84:85]
	v_add_u32_e32 v103, s13, v103
	v_max_i32_e32 v106, 0, v103
	s_add_u32 m0, s10, 0x800
	v_mad_u32_u24 v108, v106, s16, v104
	global_load_lds_dwordx4 v108, s[84:85]
	v_add_u32_e32 v103, s13, v103
	v_max_i32_e32 v106, 0, v103
	s_add_u32 m0, s10, 0xc00
	v_mad_u32_u24 v108, v106, s16, v104
	global_load_lds_dwordx4 v108, s[84:85]
	s_add_u32 s13, s11, 4
	s_cmp_eq_u32 s11, 0
	s_cselect_b32 s13, 0, s13
	s_lshl_b32 s10, s13, 5
	v_add_u32_e32 v102, s10, v101
	v_mul_u32_u24_e32 v103, s81, v102
	v_add_u32_e32 v103, s82, v103
	s_lshl_b32 s10, s13, 12
	s_add_u32 s10, s10, s12
	s_lshl_b32 s13, s81, 3
	v_max_i32_e32 v106, 0, v103
	s_mov_b32 m0, s10
	v_mad_u32_u24 v108, v106, s16, v104
	global_load_lds_dwordx4 v108, s[84:85]
	v_add_u32_e32 v103, s13, v103
	v_max_i32_e32 v106, 0, v103
	s_add_u32 m0, s10, 0x400
	v_mad_u32_u24 v108, v106, s16, v104
	global_load_lds_dwordx4 v108, s[84:85]
	v_add_u32_e32 v103, s13, v103
	v_max_i32_e32 v106, 0, v103
	s_add_u32 m0, s10, 0x800
	v_mad_u32_u24 v108, v106, s16, v104
	global_load_lds_dwordx4 v108, s[84:85]
	v_add_u32_e32 v103, s13, v103
	v_max_i32_e32 v106, 0, v103
	s_add_u32 m0, s10, 0xc00
	v_mad_u32_u24 v108, v106, s16, v104
	global_load_lds_dwordx4 v108, s[84:85]
	s_waitcnt vmcnt(0)
	s_barrier
	s_andn2_b64 vcc, exec, s[8:9]
	s_cbranch_vccz .LBB0_429
	s_branch .LBB0_492

.LBB0_431:
	s_cmp_lt_i32 s33, 1
	s_cselect_b64 s[78:79], -1, 0
	s_lshl_b32 s37, s88, 6
	ds_read_b128 v[82:85], v221 offset:32768
	ds_read_b128 v[86:89], v222 offset:32768
	ds_read_b128 v[90:93], v223 offset:32768
	ds_read_b128 v[94:97], v224 offset:32768
	ds_read_b128 v[98:101], v221 offset:36864
	ds_read_b128 v[102:105], v222 offset:36864
	ds_read_b128 v[106:109], v223 offset:36864
	ds_read_b128 v[110:113], v224 offset:36864
	v_cndmask_b32_e64 v34, 0, 1, s[78:79]
	v_cmp_ne_u32_e64 s[72:73], 1, v34
	s_waitcnt lgkmcnt(7)
	v_mfma_f32_32x32x16_bf16 v[18:33], v[82:85], v[158:161], 0
	s_waitcnt lgkmcnt(6)
	v_mfma_f32_32x32x16_bf16 v[18:33], v[86:89], v[154:157], v[18:33]
	s_waitcnt lgkmcnt(5)
	v_mfma_f32_32x32x16_bf16 v[18:33], v[90:93], v[150:153], v[18:33]
	s_waitcnt lgkmcnt(4)
	v_mfma_f32_32x32x16_bf16 v[18:33], v[94:97], v[146:149], v[18:33]
	ds_read_b128 v[82:85], v221 offset:40960
	ds_read_b128 v[86:89], v222 offset:40960
	ds_read_b128 v[90:93], v223 offset:40960
	ds_read_b128 v[94:97], v224 offset:40960
	s_waitcnt lgkmcnt(7)
	v_mfma_f32_32x32x16_bf16 v[2:17], v[98:101], v[158:161], 0
	s_waitcnt lgkmcnt(6)
	v_mfma_f32_32x32x16_bf16 v[2:17], v[102:105], v[154:157], v[2:17]
	s_waitcnt lgkmcnt(5)
	v_mfma_f32_32x32x16_bf16 v[2:17], v[106:109], v[150:153], v[2:17]
	s_waitcnt lgkmcnt(4)
	v_mfma_f32_32x32x16_bf16 v[2:17], v[110:113], v[146:149], v[2:17]
	ds_read_b128 v[98:101], v221 offset:45056
	ds_read_b128 v[102:105], v222 offset:45056
	ds_read_b128 v[106:109], v223 offset:45056
	ds_read_b128 v[110:113], v224 offset:45056
	s_waitcnt lgkmcnt(7)
	v_mfma_f32_32x32x16_bf16 v[34:49], v[82:85], v[158:161], 0
	s_waitcnt lgkmcnt(6)
	v_mfma_f32_32x32x16_bf16 v[34:49], v[86:89], v[154:157], v[34:49]
	s_waitcnt lgkmcnt(5)
	v_mfma_f32_32x32x16_bf16 v[34:49], v[90:93], v[150:153], v[34:49]
	s_waitcnt lgkmcnt(4)
	v_mfma_f32_32x32x16_bf16 v[34:49], v[94:97], v[146:149], v[34:49]
	ds_read_b128 v[82:85], v221 offset:49152
	ds_read_b128 v[86:89], v222 offset:49152
	ds_read_b128 v[90:93], v223 offset:49152
	ds_read_b128 v[94:97], v224 offset:49152
	s_waitcnt lgkmcnt(7)
	v_mfma_f32_32x32x16_bf16 v[50:65], v[98:101], v[158:161], 0
	s_waitcnt lgkmcnt(6)
	v_mfma_f32_32x32x16_bf16 v[50:65], v[102:105], v[154:157], v[50:65]
	s_waitcnt lgkmcnt(5)
	v_mfma_f32_32x32x16_bf16 v[50:65], v[106:109], v[150:153], v[50:65]
	s_waitcnt lgkmcnt(4)
	v_mfma_f32_32x32x16_bf16 v[50:65], v[110:113], v[146:149], v[50:65]
	s_waitcnt lgkmcnt(3)
	v_mfma_f32_32x32x16_bf16 v[66:81], v[82:85], v[158:161], 0
	s_waitcnt lgkmcnt(2)
	v_mfma_f32_32x32x16_bf16 v[66:81], v[86:89], v[154:157], v[66:81]
	s_waitcnt lgkmcnt(1)
	v_mfma_f32_32x32x16_bf16 v[66:81], v[90:93], v[150:153], v[66:81]
	s_waitcnt lgkmcnt(0)
	v_mfma_f32_32x32x16_bf16 v[66:81], v[94:97], v[146:149], v[66:81]
	s_barrier
	s_add_i32 s38, s53, 1
	s_cmp_lt_i32 s38, s0
	s_cselect_b64 s[96:97], -1, 0
	s_cmp_ge_i32 s38, s0
	s_mov_b32 s39, s86
	s_mov_b32 s40, s88
	s_mov_b32 s47, s81
	s_mov_b32 s41, s33
	s_mov_b32 s80, s42
	s_mov_b32 s48, s82
	v_mov_b32_e32 v183, v180
	v_mov_b32_e32 v190, v178
	v_mov_b32_e32 v187, v182
	s_cbranch_scc1 .LBB0_466
	v_readlane_b32 s40, v254, 8
	v_readlane_b32 s41, v254, 9
	s_mov_b64 s[4:5], -1
	s_and_b64 vcc, exec, s[40:41]
	s_cbranch_vccz .LBB0_454
	s_mul_i32 s4, s38, s74
	v_readlane_b32 s40, v254, 19
	s_add_i32 s39, s4, s40
	s_mov_b64 s[4:5], 0

.LBB0_461:
	v_mov_b32_e32 v89, v179
	s_nop 0
	s_nop 0
	s_nop 0
.LBB0_462:
	s_andn2_b64 vcc, exec, s[4:5]
	s_cbranch_vccnz .LBB0_490
	v_mov_b32_e32 v191, v179
	v_lshl_add_u64 v[82:83], s[84:85], 0, v[190:191]
	s_lshl_b32 s4, 48, s48
	v_mad_i64_i32 v[86:87], s[4:5], s4, v225, v[82:83]
	s_nop 0
	s_cbranch_execnz .LBB0_465
.LBB0_464:
	v_mov_b32_e32 v82, v0
	v_lshrrev_b32_e32 v83, 3, v82
	v_bfe_u32 v85, v82, 3, 3
	v_xor_b32_e32 v88, v83, v82
	v_mov_b64_e32 v[82:83], s[84:85]
	s_lshl_b32 s90, s47, 1
	v_lshlrev_b32_e32 v88, 4, v88
	v_and_b32_e32 v88, 0x70, v88
	v_mov_b32_e32 v89, v179
	s_nop 0
	v_readlane_b32 s4, v254, 34
	s_nop 0
	v_or_b32_e32 v86, s4, v85
	v_lshlrev_b32_e32 v86, s48, v86
	v_add_u32_e32 v86, s80, v86
	v_max_i32_e32 v86, 0, v86
	v_mad_u64_u32 v[86:87], s[4:5], v86, s21, v[82:83]
	v_lshl_add_u64 v[86:87], v[86:87], 0, s[90:91]
	v_lshl_add_u64 v[86:87], v[86:87], 0, v[88:89]
	v_lshl_add_u64 v[86:87], v[86:87], 0, s[92:93]
	s_nop 0
.LBB0_465:
	v_lshlrev_b32_e32 v82, s48, v1
	v_add_u32_e32 v183, s80, v82
	v_mov_b64_e32 v[82:83], s[84:85]
	v_mad_i64_i32 v[82:83], s[4:5], v183, s21, v[82:83]
	s_lshl_b32 s90, s47, 1
	v_lshl_add_u64 v[82:83], v[82:83], 0, s[90:91]
	v_mov_b32_e32 v187, v179
	v_lshl_add_u64 v[82:83], v[82:83], 0, v[186:187]
	global_load_dwordx4 v[162:165], v[82:83], off
	global_load_dwordx4 v[166:169], v[82:83], off offset:32
	global_load_dwordx4 v[170:173], v[82:83], off offset:64
	global_load_dwordx4 v[174:177], v[82:83], off offset:96
	s_lshl_b32 s4, 0xffffff80, s48
	s_lshl_b32 s47, 1, s48
	s_add_i32 s48, s80, s4
	v_add_u32_e32 v187, v208, v84
	v_and_b32_e32 v82, 63, v0
	v_lshrrev_b32_e32 v83, 3, v82
	v_and_b32_e32 v86, 7, v82
	v_xor_b32_e32 v86, v86, v83
	v_lshlrev_b32_e32 v86, 4, v86
	s_lshl_b32 s4, s40, 7
	s_add_u32 s4, s4, 0x800
	v_add_u32_e32 v86, s4, v86
	s_bfe_u32 s5, s75, 0x2000c
	s_and_b32 s53, s75, 0xffff0000
	s_add_u32 s53, s53, 0x8000
	s_add_u32 s90, s5, 1
	s_lshl_b32 s4, s90, 5
	v_add_u32_e32 v85, s4, v83
	v_mul_u32_u24_e32 v92, s47, v85
	v_add_u32_e32 v92, s48, v92
	s_lshl_b32 s4, s90, 12
	s_add_u32 s4, s4, s53
	s_lshl_b32 s90, s47, 3
	v_max_i32_e32 v88, 0, v92
	s_mov_b32 m0, s4
	v_mad_u32_u24 v90, v88, s21, v86
	global_load_lds_dwordx4 v90, s[84:85]
	v_add_u32_e32 v92, s90, v92
	v_max_i32_e32 v88, 0, v92
	s_add_u32 m0, s4, 0x400
	v_mad_u32_u24 v90, v88, s21, v86
	global_load_lds_dwordx4 v90, s[84:85]
	v_add_u32_e32 v92, s90, v92
	v_max_i32_e32 v88, 0, v92
	s_add_u32 m0, s4, 0x800
	v_mad_u32_u24 v90, v88, s21, v86
	global_load_lds_dwordx4 v90, s[84:85]
	v_add_u32_e32 v92, s90, v92
	v_max_i32_e32 v88, 0, v92
	s_add_u32 m0, s4, 0xc00
	v_mad_u32_u24 v90, v88, s21, v86
	global_load_lds_dwordx4 v90, s[84:85]
	s_add_u32 s90, s5, 4
	s_cmp_eq_u32 s5, 0
	s_cselect_b32 s90, 0, s90
	s_lshl_b32 s4, s90, 5
	v_add_u32_e32 v85, s4, v83
	v_mul_u32_u24_e32 v92, s47, v85
	v_add_u32_e32 v92, s48, v92
	s_lshl_b32 s4, s90, 12
	s_add_u32 s4, s4, s53
	s_lshl_b32 s90, s47, 3
	v_max_i32_e32 v88, 0, v92
	s_mov_b32 m0, s4
	v_mad_u32_u24 v90, v88, s21, v86
	global_load_lds_dwordx4 v90, s[84:85]
	v_add_u32_e32 v92, s90, v92
	v_max_i32_e32 v88, 0, v92
	s_add_u32 m0, s4, 0x400
	v_mad_u32_u24 v90, v88, s21, v86
	global_load_lds_dwordx4 v90, s[84:85]
	v_add_u32_e32 v92, s90, v92
	v_max_i32_e32 v88, 0, v92
	s_add_u32 m0, s4, 0x800
	v_mad_u32_u24 v90, v88, s21, v86
	global_load_lds_dwordx4 v90, s[84:85]
	v_add_u32_e32 v92, s90, v92
	v_max_i32_e32 v88, 0, v92
	s_add_u32 m0, s4, 0xc00
	v_mad_u32_u24 v90, v88, s21, v86
	global_load_lds_dwordx4 v90, s[84:85]

.LBB0_487:
	s_or_b64 exec, exec, s[4:5]
	s_waitcnt lgkmcnt(0)
	s_and_b64 vcc, exec, s[72:73]
	s_cbranch_vccnz .LBB0_430
	v_mov_b64_e32 v[146:147], v[174:175]
	v_mov_b64_e32 v[150:151], v[170:171]
	v_mov_b64_e32 v[154:155], v[166:167]
	v_mov_b64_e32 v[158:159], v[162:163]
	v_mov_b64_e32 v[148:149], v[176:177]
	v_mov_b64_e32 v[152:153], v[172:173]
	v_mov_b64_e32 v[156:157], v[168:169]
	v_mov_b64_e32 v[160:161], v[164:165]
	v_mov_b32_e32 v182, v187
	v_mov_b32_e32 v178, v190
	v_mov_b32_e32 v180, v183
	s_mov_b32 s82, s48
	s_mov_b32 s42, s80
	s_mov_b32 s33, s41
	s_mov_b32 s81, s47
	s_mov_b32 s88, s40
	s_mov_b32 s86, s39
	v_and_b32_e32 v2, 63, v0
	v_lshrrev_b32_e32 v3, 3, v2
	v_and_b32_e32 v6, 7, v2
	v_lshlrev_b32_e32 v6, 4, v6
	s_lshl_b32 s4, s88, 7
	s_add_u32 s4, s4, 0x1000
	v_add_u32_e32 v6, s4, v6
	s_bfe_u32 s5, s75, 0x2000c
	s_and_b32 s43, s75, 0xffff0000
	s_add_u32 s44, s5, 1
	s_lshl_b32 s4, s44, 5
	v_add_u32_e32 v4, s4, v3
	v_mul_u32_u24_e32 v5, s81, v4
	v_add_u32_e32 v5, s82, v5
	s_lshl_b32 s4, s44, 12
	s_add_u32 s4, s4, s43
	s_lshl_b32 s44, s81, 3
	v_max_i32_e32 v8, 0, v5
	s_mov_b32 m0, s4
	v_mad_u32_u24 v10, v8, s21, v6
	global_load_lds_dwordx4 v10, s[84:85]
	v_add_u32_e32 v5, s44, v5
	v_max_i32_e32 v8, 0, v5
	s_add_u32 m0, s4, 0x400
	v_mad_u32_u24 v10, v8, s21, v6
	global_load_lds_dwordx4 v10, s[84:85]
	v_add_u32_e32 v5, s44, v5
	v_max_i32_e32 v8, 0, v5
	s_add_u32 m0, s4, 0x800
	v_mad_u32_u24 v10, v8, s21, v6
	global_load_lds_dwordx4 v10, s[84:85]
	v_add_u32_e32 v5, s44, v5
	v_max_i32_e32 v8, 0, v5
	s_add_u32 m0, s4, 0xc00
	v_mad_u32_u24 v10, v8, s21, v6
	global_load_lds_dwordx4 v10, s[84:85]
	s_add_u32 s44, s5, 4
	s_cmp_eq_u32 s5, 0
	s_cselect_b32 s44, 0, s44
	s_lshl_b32 s4, s44, 5
	v_add_u32_e32 v4, s4, v3
	v_mul_u32_u24_e32 v5, s81, v4
	v_add_u32_e32 v5, s82, v5
	s_lshl_b32 s4, s44, 12
	s_add_u32 s4, s4, s43
	s_lshl_b32 s44, s81, 3
	v_max_i32_e32 v8, 0, v5
	s_mov_b32 m0, s4
	v_mad_u32_u24 v10, v8, s21, v6
	global_load_lds_dwordx4 v10, s[84:85]
	v_add_u32_e32 v5, s44, v5
	v_max_i32_e32 v8, 0, v5
	s_add_u32 m0, s4, 0x400
	v_mad_u32_u24 v10, v8, s21, v6
	global_load_lds_dwordx4 v10, s[84:85]
	v_add_u32_e32 v5, s44, v5
	v_max_i32_e32 v8, 0, v5
	s_add_u32 m0, s4, 0x800
	v_mad_u32_u24 v10, v8, s21, v6
	global_load_lds_dwordx4 v10, s[84:85]
	v_add_u32_e32 v5, s44, v5
	v_max_i32_e32 v8, 0, v5
	s_add_u32 m0, s4, 0xc00
	v_mad_u32_u24 v10, v8, s21, v6
	global_load_lds_dwordx4 v10, s[84:85]
	s_branch .LBB0_430
